# kvq-projection norm epilogue: the 32 dependent ds_bpermute round trips per unit batched (counted lgkmcnt), on top of prep-loop rewrite + new conversion queue
# speedup vs baseline: 1.0107x; 1.0107x over previous
.LBB0_1037:
	ds_read_b128 v[130:133], v192
	ds_read_b128 v[134:137], v192 offset:1024
	ds_read_b128 v[200:203], v192 offset:2048
	ds_read_b128 v[204:207], v192 offset:3072
	s_add_u32 s8, s4, 0xfff80080
	s_addc_u32 s9, s5, -1
	s_cmp_eq_u32 s67, 28
	s_cselect_b32 s55, s17, s9
	s_cselect_b32 s54, s63, s8
	s_cselect_b32 s9, s15, s66
	s_cselect_b32 s8, s64, s65
	v_lshl_add_u64 v[150:151], s[4:5], 0, v[146:147]
	s_add_i32 m0, s23, 0xc000
	ds_read_b128 v[208:211], v193
	ds_read_b128 v[212:215], v193 offset:1024
	ds_read_b128 v[220:223], v193 offset:2048
	ds_read_b128 v[224:227], v193 offset:3072
	ds_read_b128 v[228:231], v193 offset:4096
	ds_read_b128 v[232:235], v193 offset:5120
	ds_read_b128 v[236:239], v193 offset:6144
	ds_read_b128 v[240:243], v193 offset:7168
	global_load_lds_dwordx4 v[150:151], off
	v_lshl_add_u64 v[150:151], s[4:5], 0, v[148:149]
	s_add_i32 m0, s23, 0xe000
	s_nop 0
	global_load_lds_dwordx4 v[150:151], off
	s_waitcnt lgkmcnt(8)
	s_barrier
	s_waitcnt lgkmcnt(0)
	s_setprio 1
	s_waitcnt lgkmcnt(0)
	v_mfma_f32_16x16x32_bf16 v[126:129], v[130:133], v[208:211], v[126:129]
	v_mfma_f32_16x16x32_bf16 v[122:125], v[200:203], v[208:211], v[122:125]
	v_mfma_f32_16x16x32_bf16 v[110:113], v[130:133], v[220:223], v[110:113]
	v_mfma_f32_16x16x32_bf16 v[106:109], v[200:203], v[220:223], v[106:109]
	v_mfma_f32_16x16x32_bf16 v[94:97], v[130:133], v[228:231], v[94:97]
	v_mfma_f32_16x16x32_bf16 v[90:93], v[200:203], v[228:231], v[90:93]
	v_mfma_f32_16x16x32_bf16 v[78:81], v[130:133], v[236:239], v[78:81]
	v_mfma_f32_16x16x32_bf16 v[74:77], v[200:203], v[236:239], v[74:77]
	v_mfma_f32_16x16x32_bf16 v[126:129], v[134:137], v[212:215], v[126:129]
	v_mfma_f32_16x16x32_bf16 v[122:125], v[204:207], v[212:215], v[122:125]
	v_mfma_f32_16x16x32_bf16 v[110:113], v[134:137], v[224:227], v[110:113]
	v_mfma_f32_16x16x32_bf16 v[106:109], v[204:207], v[224:227], v[106:109]
	v_mfma_f32_16x16x32_bf16 v[94:97], v[134:137], v[232:235], v[94:97]
	v_mfma_f32_16x16x32_bf16 v[90:93], v[204:207], v[232:235], v[90:93]
	v_mfma_f32_16x16x32_bf16 v[78:81], v[134:137], v[240:243], v[78:81]
	v_mfma_f32_16x16x32_bf16 v[74:77], v[204:207], v[240:243], v[74:77]
	s_setprio 0
	s_barrier
	s_add_i32 s68, s58, s3
	v_lshl_add_u64 v[186:187], s[8:9], 0, v[140:141]
	s_mov_b32 m0, s68
	ds_read_b128 v[244:247], v194
	ds_read_b128 v[248:251], v194 offset:1024
	ds_read_b128 v[150:153], v194 offset:2048
	ds_read_b128 v[176:179], v194 offset:3072
	global_load_lds_dwordx4 v[186:187], off
	v_lshl_add_u64 v[216:217], s[8:9], 0, v[144:145]
	s_add_i32 m0, s68, 0x2000
	s_nop 0
	global_load_lds_dwordx4 v[216:217], off
	s_barrier
	s_waitcnt lgkmcnt(0)
	s_setprio 1
	s_waitcnt lgkmcnt(0)
	v_mfma_f32_16x16x32_bf16 v[118:121], v[244:247], v[208:211], v[118:121]
	v_mfma_f32_16x16x32_bf16 v[114:117], v[150:153], v[208:211], v[114:117]
	v_mfma_f32_16x16x32_bf16 v[102:105], v[244:247], v[220:223], v[102:105]
	v_mfma_f32_16x16x32_bf16 v[98:101], v[150:153], v[220:223], v[98:101]
	v_mfma_f32_16x16x32_bf16 v[86:89], v[244:247], v[228:231], v[86:89]
	v_mfma_f32_16x16x32_bf16 v[82:85], v[150:153], v[228:231], v[82:85]
	v_mfma_f32_16x16x32_bf16 v[70:73], v[244:247], v[236:239], v[70:73]
	v_mfma_f32_16x16x32_bf16 v[66:69], v[150:153], v[236:239], v[66:69]
	v_mfma_f32_16x16x32_bf16 v[118:121], v[248:251], v[212:215], v[118:121]
	v_mfma_f32_16x16x32_bf16 v[114:117], v[176:179], v[212:215], v[114:117]
	v_mfma_f32_16x16x32_bf16 v[102:105], v[248:251], v[224:227], v[102:105]
	v_mfma_f32_16x16x32_bf16 v[98:101], v[176:179], v[224:227], v[98:101]
	v_mfma_f32_16x16x32_bf16 v[86:89], v[248:251], v[232:235], v[86:89]
	v_mfma_f32_16x16x32_bf16 v[82:85], v[176:179], v[232:235], v[82:85]
	v_mfma_f32_16x16x32_bf16 v[70:73], v[248:251], v[240:243], v[70:73]
	v_mfma_f32_16x16x32_bf16 v[66:69], v[176:179], v[240:243], v[66:69]
	s_setprio 0
	s_mov_b32 m0, s23
	v_lshl_add_u64 v[252:253], s[54:55], 0, v[138:139]
	s_barrier
	ds_read_b128 v[208:211], v193 offset:16384
	ds_read_b128 v[212:215], v193 offset:17408
	ds_read_b128 v[220:223], v193 offset:18432
	ds_read_b128 v[224:227], v193 offset:19456
	ds_read_b128 v[228:231], v193 offset:20480
	ds_read_b128 v[232:235], v193 offset:21504
	ds_read_b128 v[236:239], v193 offset:22528
	ds_read_b128 v[240:243], v193 offset:23552
	global_load_lds_dwordx4 v[252:253], off
	v_lshl_add_u64 v[160:161], s[54:55], 0, v[142:143]
	s_mov_b32 m0, s25
	s_nop 0
	global_load_lds_dwordx4 v[160:161], off
	s_barrier
	s_waitcnt lgkmcnt(0)
	s_setprio 1
	s_waitcnt lgkmcnt(0)
	v_mfma_f32_16x16x32_bf16 v[62:65], v[130:133], v[208:211], v[62:65]
	v_mfma_f32_16x16x32_bf16 v[58:61], v[200:203], v[208:211], v[58:61]
	v_mfma_f32_16x16x32_bf16 v[46:49], v[130:133], v[220:223], v[46:49]
	v_mfma_f32_16x16x32_bf16 v[42:45], v[200:203], v[220:223], v[42:45]
	v_mfma_f32_16x16x32_bf16 v[30:33], v[130:133], v[228:231], v[30:33]
	v_mfma_f32_16x16x32_bf16 v[26:29], v[200:203], v[228:231], v[26:29]
	v_mfma_f32_16x16x32_bf16 v[14:17], v[130:133], v[236:239], v[14:17]
	v_mfma_f32_16x16x32_bf16 v[10:13], v[200:203], v[236:239], v[10:13]
	v_mfma_f32_16x16x32_bf16 v[62:65], v[134:137], v[212:215], v[62:65]
	v_mfma_f32_16x16x32_bf16 v[58:61], v[204:207], v[212:215], v[58:61]
	v_mfma_f32_16x16x32_bf16 v[46:49], v[134:137], v[224:227], v[46:49]
	v_mfma_f32_16x16x32_bf16 v[42:45], v[204:207], v[224:227], v[42:45]
	v_mfma_f32_16x16x32_bf16 v[30:33], v[134:137], v[232:235], v[30:33]
	v_mfma_f32_16x16x32_bf16 v[26:29], v[204:207], v[232:235], v[26:29]
	v_mfma_f32_16x16x32_bf16 v[14:17], v[134:137], v[240:243], v[14:17]
	v_mfma_f32_16x16x32_bf16 v[10:13], v[204:207], v[240:243], v[10:13]
	s_setprio 0
	s_barrier
	s_add_u32 s68, s8, 0x80000
	s_addc_u32 s69, s9, 0
	s_add_i32 s72, s59, s3
	v_lshl_add_u64 v[130:131], s[68:69], 0, v[140:141]
	s_mov_b32 m0, s72
	s_nop 0
	global_load_lds_dwordx4 v[130:131], off
	v_lshl_add_u64 v[130:131], s[68:69], 0, v[144:145]
	s_add_i32 m0, s72, 0x2000
	s_nop 0
	global_load_lds_dwordx4 v[130:131], off
	s_waitcnt vmcnt(6)
	s_barrier
	s_setprio 1
	v_mfma_f32_16x16x32_bf16 v[54:57], v[244:247], v[208:211], v[54:57]
	v_mfma_f32_16x16x32_bf16 v[50:53], v[150:153], v[208:211], v[50:53]
	v_mfma_f32_16x16x32_bf16 v[38:41], v[244:247], v[220:223], v[38:41]
	v_mfma_f32_16x16x32_bf16 v[34:37], v[150:153], v[220:223], v[34:37]
	v_mfma_f32_16x16x32_bf16 v[22:25], v[244:247], v[228:231], v[22:25]
	v_mfma_f32_16x16x32_bf16 v[18:21], v[150:153], v[228:231], v[18:21]
	v_mfma_f32_16x16x32_bf16 v[6:9], v[244:247], v[236:239], v[6:9]
	v_mfma_f32_16x16x32_bf16 v[2:5], v[150:153], v[236:239], v[2:5]
	v_mfma_f32_16x16x32_bf16 v[54:57], v[248:251], v[212:215], v[54:57]
	v_mfma_f32_16x16x32_bf16 v[50:53], v[176:179], v[212:215], v[50:53]
	v_mfma_f32_16x16x32_bf16 v[38:41], v[248:251], v[224:227], v[38:41]
	v_mfma_f32_16x16x32_bf16 v[34:37], v[176:179], v[224:227], v[34:37]
	v_mfma_f32_16x16x32_bf16 v[22:25], v[248:251], v[232:235], v[22:25]
	v_mfma_f32_16x16x32_bf16 v[18:21], v[176:179], v[232:235], v[18:21]
	v_mfma_f32_16x16x32_bf16 v[6:9], v[248:251], v[240:243], v[6:9]
	v_mfma_f32_16x16x32_bf16 v[2:5], v[176:179], v[240:243], v[2:5]
	s_setprio 0
	s_add_i32 s68, 0, 0x18000
	v_add_u32_e32 v154, s68, v157
	s_barrier
	ds_read_b128 v[130:133], v154
	ds_read_b128 v[134:137], v154 offset:1024
	ds_read_b128 v[150:153], v154 offset:2048
	ds_read_b128 v[176:179], v154 offset:3072
	s_add_u32 s54, s54, 0x80000
	s_addc_u32 s55, s55, 0
	s_mov_b32 m0, s26
	v_lshl_add_u64 v[236:237], s[54:55], 0, v[138:139]
	ds_read_b128 v[200:203], v193 offset:32768
	ds_read_b128 v[204:207], v193 offset:33792
	ds_read_b128 v[208:211], v193 offset:34816
	ds_read_b128 v[212:215], v193 offset:35840
	ds_read_b128 v[220:223], v193 offset:36864
	ds_read_b128 v[224:227], v193 offset:37888
	ds_read_b128 v[228:231], v193 offset:38912
	ds_read_b128 v[232:235], v193 offset:39936
	global_load_lds_dwordx4 v[236:237], off
	v_lshl_add_u64 v[236:237], s[54:55], 0, v[142:143]
	s_mov_b32 m0, s33
	s_nop 0
	global_load_lds_dwordx4 v[236:237], off
	s_waitcnt lgkmcnt(8)
	s_barrier
	s_waitcnt lgkmcnt(0)
	s_setprio 1
	s_waitcnt lgkmcnt(0)
	v_mfma_f32_16x16x32_bf16 v[126:129], v[130:133], v[200:203], v[126:129]
	v_mfma_f32_16x16x32_bf16 v[122:125], v[150:153], v[200:203], v[122:125]
	v_mfma_f32_16x16x32_bf16 v[110:113], v[130:133], v[208:211], v[110:113]
	v_mfma_f32_16x16x32_bf16 v[106:109], v[150:153], v[208:211], v[106:109]
	v_mfma_f32_16x16x32_bf16 v[94:97], v[130:133], v[220:223], v[94:97]
	v_mfma_f32_16x16x32_bf16 v[90:93], v[150:153], v[220:223], v[90:93]
	v_mfma_f32_16x16x32_bf16 v[78:81], v[130:133], v[228:231], v[78:81]
	v_mfma_f32_16x16x32_bf16 v[74:77], v[150:153], v[228:231], v[74:77]
	v_mfma_f32_16x16x32_bf16 v[126:129], v[134:137], v[204:207], v[126:129]
	v_mfma_f32_16x16x32_bf16 v[122:125], v[176:179], v[204:207], v[122:125]
	v_mfma_f32_16x16x32_bf16 v[110:113], v[134:137], v[212:215], v[110:113]
	v_mfma_f32_16x16x32_bf16 v[106:109], v[176:179], v[212:215], v[106:109]
	v_mfma_f32_16x16x32_bf16 v[94:97], v[134:137], v[224:227], v[94:97]
	v_mfma_f32_16x16x32_bf16 v[90:93], v[176:179], v[224:227], v[90:93]
	v_mfma_f32_16x16x32_bf16 v[78:81], v[134:137], v[232:235], v[78:81]
	v_mfma_f32_16x16x32_bf16 v[74:77], v[176:179], v[232:235], v[74:77]
	s_setprio 0
	s_barrier
	s_add_i32 s54, 0, 0x1c000
	s_add_i32 s55, s68, s3
	v_add_u32_e32 v154, s54, v157
	v_lshl_add_u64 v[186:187], v[186:187], 0, s[12:13]
	s_mov_b32 m0, s55
	ds_read_b128 v[236:239], v154
	ds_read_b128 v[240:243], v154 offset:1024
	ds_read_b128 v[244:247], v154 offset:2048
	ds_read_b128 v[248:251], v154 offset:3072
	global_load_lds_dwordx4 v[186:187], off
	v_lshl_add_u64 v[186:187], v[216:217], 0, s[12:13]
	s_add_i32 m0, s55, 0x2000
	s_nop 0
	global_load_lds_dwordx4 v[186:187], off
	s_barrier
	s_waitcnt lgkmcnt(0)
	s_setprio 1
	s_waitcnt lgkmcnt(0)
	v_mfma_f32_16x16x32_bf16 v[118:121], v[236:239], v[200:203], v[118:121]
	v_mfma_f32_16x16x32_bf16 v[114:117], v[244:247], v[200:203], v[114:117]
	v_mfma_f32_16x16x32_bf16 v[102:105], v[236:239], v[208:211], v[102:105]
	v_mfma_f32_16x16x32_bf16 v[98:101], v[244:247], v[208:211], v[98:101]
	v_mfma_f32_16x16x32_bf16 v[86:89], v[236:239], v[220:223], v[86:89]
	v_mfma_f32_16x16x32_bf16 v[82:85], v[244:247], v[220:223], v[82:85]
	v_mfma_f32_16x16x32_bf16 v[70:73], v[236:239], v[228:231], v[70:73]
	v_mfma_f32_16x16x32_bf16 v[66:69], v[244:247], v[228:231], v[66:69]
	v_mfma_f32_16x16x32_bf16 v[118:121], v[240:243], v[204:207], v[118:121]
	v_mfma_f32_16x16x32_bf16 v[114:117], v[248:251], v[204:207], v[114:117]
	v_mfma_f32_16x16x32_bf16 v[102:105], v[240:243], v[212:215], v[102:105]
	v_mfma_f32_16x16x32_bf16 v[98:101], v[248:251], v[212:215], v[98:101]
	v_mfma_f32_16x16x32_bf16 v[86:89], v[240:243], v[224:227], v[86:89]
	v_mfma_f32_16x16x32_bf16 v[82:85], v[248:251], v[224:227], v[82:85]
	v_mfma_f32_16x16x32_bf16 v[70:73], v[240:243], v[232:235], v[70:73]
	v_mfma_f32_16x16x32_bf16 v[66:69], v[248:251], v[232:235], v[66:69]
	s_setprio 0
	s_mov_b32 m0, s35
	v_lshl_add_u64 v[186:187], v[252:253], 0, s[12:13]
	s_barrier
	ds_read_b128 v[200:203], v193 offset:49152
	ds_read_b128 v[204:207], v193 offset:50176
	ds_read_b128 v[208:211], v193 offset:51200
	ds_read_b128 v[212:215], v193 offset:52224
	ds_read_b128 v[220:223], v193 offset:53248
	ds_read_b128 v[224:227], v193 offset:54272
	ds_read_b128 v[228:231], v193 offset:55296
	ds_read_b128 v[232:235], v193 offset:56320
	global_load_lds_dwordx4 v[186:187], off
	v_lshl_add_u64 v[160:161], v[160:161], 0, s[12:13]
	s_mov_b32 m0, s40
	s_nop 0
	global_load_lds_dwordx4 v[160:161], off
	s_barrier
	s_waitcnt lgkmcnt(0)
	s_setprio 1
	s_waitcnt lgkmcnt(0)
	v_mfma_f32_16x16x32_bf16 v[62:65], v[130:133], v[200:203], v[62:65]
	v_mfma_f32_16x16x32_bf16 v[58:61], v[150:153], v[200:203], v[58:61]
	v_mfma_f32_16x16x32_bf16 v[46:49], v[130:133], v[208:211], v[46:49]
	v_mfma_f32_16x16x32_bf16 v[42:45], v[150:153], v[208:211], v[42:45]
	v_mfma_f32_16x16x32_bf16 v[30:33], v[130:133], v[220:223], v[30:33]
	v_mfma_f32_16x16x32_bf16 v[26:29], v[150:153], v[220:223], v[26:29]
	v_mfma_f32_16x16x32_bf16 v[14:17], v[130:133], v[228:231], v[14:17]
	v_mfma_f32_16x16x32_bf16 v[10:13], v[150:153], v[228:231], v[10:13]
	v_mfma_f32_16x16x32_bf16 v[62:65], v[134:137], v[204:207], v[62:65]
	v_mfma_f32_16x16x32_bf16 v[58:61], v[176:179], v[204:207], v[58:61]
	v_mfma_f32_16x16x32_bf16 v[46:49], v[134:137], v[212:215], v[46:49]
	v_mfma_f32_16x16x32_bf16 v[42:45], v[176:179], v[212:215], v[42:45]
	v_mfma_f32_16x16x32_bf16 v[30:33], v[134:137], v[224:227], v[30:33]
	v_mfma_f32_16x16x32_bf16 v[26:29], v[176:179], v[224:227], v[26:29]
	v_mfma_f32_16x16x32_bf16 v[14:17], v[134:137], v[232:235], v[14:17]
	v_mfma_f32_16x16x32_bf16 v[10:13], v[176:179], v[232:235], v[10:13]
	s_setprio 0
	s_barrier
	s_add_u32 s8, s8, 0x80080
	s_addc_u32 s9, s9, 0
	s_add_i32 s54, s54, s3
	v_lshl_add_u64 v[130:131], s[8:9], 0, v[140:141]
	s_mov_b32 m0, s54
	s_nop 0
	global_load_lds_dwordx4 v[130:131], off
	v_lshl_add_u64 v[130:131], s[8:9], 0, v[144:145]
	s_add_i32 m0, s54, 0x2000
	s_nop 0
	global_load_lds_dwordx4 v[130:131], off
	s_waitcnt vmcnt(6)
	s_barrier
	s_setprio 1
	v_mfma_f32_16x16x32_bf16 v[54:57], v[236:239], v[200:203], v[54:57]
	v_mfma_f32_16x16x32_bf16 v[50:53], v[244:247], v[200:203], v[50:53]
	v_mfma_f32_16x16x32_bf16 v[38:41], v[236:239], v[208:211], v[38:41]
	v_mfma_f32_16x16x32_bf16 v[34:37], v[244:247], v[208:211], v[34:37]
	v_mfma_f32_16x16x32_bf16 v[22:25], v[236:239], v[220:223], v[22:25]
	v_mfma_f32_16x16x32_bf16 v[18:21], v[244:247], v[220:223], v[18:21]
	v_mfma_f32_16x16x32_bf16 v[6:9], v[236:239], v[228:231], v[6:9]
	v_mfma_f32_16x16x32_bf16 v[2:5], v[244:247], v[228:231], v[2:5]
	v_mfma_f32_16x16x32_bf16 v[54:57], v[240:243], v[204:207], v[54:57]
	v_mfma_f32_16x16x32_bf16 v[50:53], v[248:251], v[204:207], v[50:53]
	v_mfma_f32_16x16x32_bf16 v[38:41], v[240:243], v[212:215], v[38:41]
	v_mfma_f32_16x16x32_bf16 v[34:37], v[248:251], v[212:215], v[34:37]
	v_mfma_f32_16x16x32_bf16 v[22:25], v[240:243], v[224:227], v[22:25]
	v_mfma_f32_16x16x32_bf16 v[18:21], v[248:251], v[224:227], v[18:21]
	v_mfma_f32_16x16x32_bf16 v[6:9], v[240:243], v[232:235], v[6:9]
	v_mfma_f32_16x16x32_bf16 v[2:5], v[248:251], v[232:235], v[2:5]
	s_setprio 0
	s_add_i32 s67, s67, 2
	s_add_u32 s4, s4, 0x100
	s_addc_u32 s5, s5, 0
	s_add_u32 s65, s65, 0x100
	s_addc_u32 s66, s66, 0
	s_cmp_gt_u32 s67, 29
	s_barrier
	s_cbranch_scc0 .LBB0_1037
	s_add_i32 s4, s22, -16
	v_mov_b32_e32 v133, 1.0
	s_cmp_lt_u32 s4, -8
	s_cselect_b64 s[54:55], -1, 0
	s_cmp_gt_u32 s4, -9
	v_mov_b32_e32 v132, 1.0
	v_mov_b32_e32 v131, 1.0
	v_mov_b32_e32 v130, v133
	v_mov_b32_e32 v137, 1.0
	v_mov_b32_e32 v136, 1.0
	v_mov_b32_e32 v135, 1.0
	v_mov_b32_e32 v134, v133
	s_cbranch_scc1 .LBB0_1072
	v_and_b32_e32 v131, 64, v198
	v_xor_b32_e32 v130, 16, v198
	v_add_u32_e32 v131, 64, v131
	v_xor_b32_e32 v134, 32, v198
	v_cmp_lt_i32_e32 vcc, v130, v131
	v_cmp_lt_i32_e64 s[4:5], v134, v131
	s_nop 1
	v_cndmask_b32_e32 v130, v198, v130, vcc
	v_cndmask_b32_e64 v131, v198, v134, s[4:5]
	v_lshlrev_b32_e32 v130, 2, v130
	v_lshlrev_b32_e32 v131, 2, v131
	v_mul_f32_e32 v220, v127, v127
	v_mul_f32_e32 v236, v129, v129
	v_fmac_f32_e32 v220, v126, v126
	v_fmac_f32_e32 v236, v128, v128
	v_add_f32_e32 v220, v220, v236
	v_mul_f32_e32 v236, v123, v123
	v_fmac_f32_e32 v236, v122, v122
	v_add_f32_e32 v220, v220, v236
	v_mul_f32_e32 v236, v125, v125
	v_fmac_f32_e32 v236, v124, v124
	v_add_f32_e32 v220, v236, v220
	v_mul_f32_e32 v221, v119, v119
	v_mul_f32_e32 v237, v121, v121
	v_fmac_f32_e32 v221, v118, v118
	v_fmac_f32_e32 v237, v120, v120
	v_add_f32_e32 v221, v221, v237
	v_mul_f32_e32 v237, v115, v115
	v_fmac_f32_e32 v237, v114, v114
	v_add_f32_e32 v221, v221, v237
	v_mul_f32_e32 v237, v117, v117
	v_fmac_f32_e32 v237, v116, v116
	v_add_f32_e32 v221, v237, v221
	v_mul_f32_e32 v222, v111, v111
	v_mul_f32_e32 v238, v113, v113
	v_fmac_f32_e32 v222, v110, v110
	v_fmac_f32_e32 v238, v112, v112
	v_add_f32_e32 v222, v222, v238
	v_mul_f32_e32 v238, v107, v107
	v_fmac_f32_e32 v238, v106, v106
	v_add_f32_e32 v222, v222, v238
	v_mul_f32_e32 v238, v109, v109
	v_fmac_f32_e32 v238, v108, v108
	v_add_f32_e32 v222, v238, v222
	v_mul_f32_e32 v223, v103, v103
	v_mul_f32_e32 v239, v105, v105
	v_fmac_f32_e32 v223, v102, v102
	v_fmac_f32_e32 v239, v104, v104
	v_add_f32_e32 v223, v223, v239
	v_mul_f32_e32 v239, v99, v99
	v_fmac_f32_e32 v239, v98, v98
	v_add_f32_e32 v223, v223, v239
	v_mul_f32_e32 v239, v101, v101
	v_fmac_f32_e32 v239, v100, v100
	v_add_f32_e32 v223, v239, v223
	v_mul_f32_e32 v224, v95, v95
	v_mul_f32_e32 v240, v97, v97
	v_fmac_f32_e32 v224, v94, v94
	v_fmac_f32_e32 v240, v96, v96
	v_add_f32_e32 v224, v224, v240
	v_mul_f32_e32 v240, v91, v91
	v_fmac_f32_e32 v240, v90, v90
	v_add_f32_e32 v224, v224, v240
	v_mul_f32_e32 v240, v93, v93
	v_fmac_f32_e32 v240, v92, v92
	v_add_f32_e32 v224, v240, v224
	v_mul_f32_e32 v225, v87, v87
	v_mul_f32_e32 v241, v89, v89
	v_fmac_f32_e32 v225, v86, v86
	v_fmac_f32_e32 v241, v88, v88
	v_add_f32_e32 v225, v225, v241
	v_mul_f32_e32 v241, v83, v83
	v_fmac_f32_e32 v241, v82, v82
	v_add_f32_e32 v225, v225, v241
	v_mul_f32_e32 v241, v85, v85
	v_fmac_f32_e32 v241, v84, v84
	v_add_f32_e32 v225, v241, v225
	v_mul_f32_e32 v226, v79, v79
	v_mul_f32_e32 v242, v81, v81
	v_fmac_f32_e32 v226, v78, v78
	v_fmac_f32_e32 v242, v80, v80
	v_add_f32_e32 v226, v226, v242
	v_mul_f32_e32 v242, v75, v75
	v_fmac_f32_e32 v242, v74, v74
	v_add_f32_e32 v226, v226, v242
	v_mul_f32_e32 v242, v77, v77
	v_fmac_f32_e32 v242, v76, v76
	v_add_f32_e32 v226, v242, v226
	v_mul_f32_e32 v227, v71, v71
	v_mul_f32_e32 v243, v73, v73
	v_fmac_f32_e32 v227, v70, v70
	v_fmac_f32_e32 v243, v72, v72
	v_add_f32_e32 v227, v227, v243
	v_mul_f32_e32 v243, v67, v67
	v_fmac_f32_e32 v243, v66, v66
	v_add_f32_e32 v227, v227, v243
	v_mul_f32_e32 v243, v69, v69
	v_fmac_f32_e32 v243, v68, v68
	v_add_f32_e32 v227, v243, v227
	v_mul_f32_e32 v228, v63, v63
	v_mul_f32_e32 v244, v65, v65
	v_fmac_f32_e32 v228, v62, v62
	v_fmac_f32_e32 v244, v64, v64
	v_add_f32_e32 v228, v228, v244
	v_mul_f32_e32 v244, v59, v59
	v_fmac_f32_e32 v244, v58, v58
	v_add_f32_e32 v228, v228, v244
	v_mul_f32_e32 v244, v61, v61
	v_fmac_f32_e32 v244, v60, v60
	v_add_f32_e32 v228, v244, v228
	v_mul_f32_e32 v229, v55, v55
	v_mul_f32_e32 v245, v57, v57
	v_fmac_f32_e32 v229, v54, v54
	v_fmac_f32_e32 v245, v56, v56
	v_add_f32_e32 v229, v229, v245
	v_mul_f32_e32 v245, v51, v51
	v_fmac_f32_e32 v245, v50, v50
	v_add_f32_e32 v229, v229, v245
	v_mul_f32_e32 v245, v53, v53
	v_fmac_f32_e32 v245, v52, v52
	v_add_f32_e32 v229, v245, v229
	v_mul_f32_e32 v230, v47, v47
	v_mul_f32_e32 v246, v49, v49
	v_fmac_f32_e32 v230, v46, v46
	v_fmac_f32_e32 v246, v48, v48
	v_add_f32_e32 v230, v230, v246
	v_mul_f32_e32 v246, v43, v43
	v_fmac_f32_e32 v246, v42, v42
	v_add_f32_e32 v230, v230, v246
	v_mul_f32_e32 v246, v45, v45
	v_fmac_f32_e32 v246, v44, v44
	v_add_f32_e32 v230, v246, v230
	v_mul_f32_e32 v231, v39, v39
	v_mul_f32_e32 v247, v41, v41
	v_fmac_f32_e32 v231, v38, v38
	v_fmac_f32_e32 v247, v40, v40
	v_add_f32_e32 v231, v231, v247
	v_mul_f32_e32 v247, v35, v35
	v_fmac_f32_e32 v247, v34, v34
	v_add_f32_e32 v231, v231, v247
	v_mul_f32_e32 v247, v37, v37
	v_fmac_f32_e32 v247, v36, v36
	v_add_f32_e32 v231, v247, v231
	v_mul_f32_e32 v232, v31, v31
	v_mul_f32_e32 v248, v33, v33
	v_fmac_f32_e32 v232, v30, v30
	v_fmac_f32_e32 v248, v32, v32
	v_add_f32_e32 v232, v232, v248
	v_mul_f32_e32 v248, v27, v27
	v_fmac_f32_e32 v248, v26, v26
	v_add_f32_e32 v232, v232, v248
	v_mul_f32_e32 v248, v29, v29
	v_fmac_f32_e32 v248, v28, v28
	v_add_f32_e32 v232, v248, v232
	v_mul_f32_e32 v233, v23, v23
	v_mul_f32_e32 v249, v25, v25
	v_fmac_f32_e32 v233, v22, v22
	v_fmac_f32_e32 v249, v24, v24
	v_add_f32_e32 v233, v233, v249
	v_mul_f32_e32 v249, v19, v19
	v_fmac_f32_e32 v249, v18, v18
	v_add_f32_e32 v233, v233, v249
	v_mul_f32_e32 v249, v21, v21
	v_fmac_f32_e32 v249, v20, v20
	v_add_f32_e32 v233, v249, v233
	v_mul_f32_e32 v234, v15, v15
	v_mul_f32_e32 v250, v17, v17
	v_fmac_f32_e32 v234, v14, v14
	v_fmac_f32_e32 v250, v16, v16
	v_add_f32_e32 v234, v234, v250
	v_mul_f32_e32 v250, v11, v11
	v_fmac_f32_e32 v250, v10, v10
	v_add_f32_e32 v234, v234, v250
	v_mul_f32_e32 v250, v13, v13
	v_fmac_f32_e32 v250, v12, v12
	v_add_f32_e32 v234, v250, v234
	v_mul_f32_e32 v235, v7, v7
	v_mul_f32_e32 v251, v9, v9
	v_fmac_f32_e32 v235, v6, v6
	v_fmac_f32_e32 v251, v8, v8
	v_add_f32_e32 v235, v235, v251
	v_mul_f32_e32 v251, v3, v3
	v_fmac_f32_e32 v251, v2, v2
	v_add_f32_e32 v235, v235, v251
	v_mul_f32_e32 v251, v5, v5
	v_fmac_f32_e32 v251, v4, v4
	v_add_f32_e32 v235, v251, v235
	ds_bpermute_b32 v236, v130, v220
	ds_bpermute_b32 v237, v130, v221
	ds_bpermute_b32 v238, v130, v222
	ds_bpermute_b32 v239, v130, v223
	ds_bpermute_b32 v240, v130, v224
	ds_bpermute_b32 v241, v130, v225
	ds_bpermute_b32 v242, v130, v226
	ds_bpermute_b32 v243, v130, v227
	s_waitcnt lgkmcnt(7)
	v_add_f32_e32 v220, v220, v236
	s_waitcnt lgkmcnt(6)
	v_add_f32_e32 v221, v221, v237
	s_waitcnt lgkmcnt(5)
	v_add_f32_e32 v222, v222, v238
	s_waitcnt lgkmcnt(4)
	v_add_f32_e32 v223, v223, v239
	s_waitcnt lgkmcnt(3)
	v_add_f32_e32 v224, v224, v240
	s_waitcnt lgkmcnt(2)
	v_add_f32_e32 v225, v225, v241
	s_waitcnt lgkmcnt(1)
	v_add_f32_e32 v226, v226, v242
	s_waitcnt lgkmcnt(0)
	v_add_f32_e32 v227, v227, v243
	ds_bpermute_b32 v244, v130, v228
	ds_bpermute_b32 v245, v130, v229
	ds_bpermute_b32 v246, v130, v230
	ds_bpermute_b32 v247, v130, v231
	ds_bpermute_b32 v248, v130, v232
	ds_bpermute_b32 v249, v130, v233
	ds_bpermute_b32 v250, v130, v234
	ds_bpermute_b32 v251, v130, v235
	s_waitcnt lgkmcnt(7)
	v_add_f32_e32 v228, v228, v244
	s_waitcnt lgkmcnt(6)
	v_add_f32_e32 v229, v229, v245
	s_waitcnt lgkmcnt(5)
	v_add_f32_e32 v230, v230, v246
	s_waitcnt lgkmcnt(4)
	v_add_f32_e32 v231, v231, v247
	s_waitcnt lgkmcnt(3)
	v_add_f32_e32 v232, v232, v248
	s_waitcnt lgkmcnt(2)
	v_add_f32_e32 v233, v233, v249
	s_waitcnt lgkmcnt(1)
	v_add_f32_e32 v234, v234, v250
	s_waitcnt lgkmcnt(0)
	v_add_f32_e32 v235, v235, v251
	ds_bpermute_b32 v236, v131, v220
	ds_bpermute_b32 v237, v131, v221
	ds_bpermute_b32 v238, v131, v222
	ds_bpermute_b32 v239, v131, v223
	ds_bpermute_b32 v240, v131, v224
	ds_bpermute_b32 v241, v131, v225
	ds_bpermute_b32 v242, v131, v226
	ds_bpermute_b32 v243, v131, v227
	s_waitcnt lgkmcnt(7)
	v_add_f32_e32 v220, v220, v236
	s_waitcnt lgkmcnt(6)
	v_add_f32_e32 v221, v221, v237
	s_waitcnt lgkmcnt(5)
	v_add_f32_e32 v222, v222, v238
	s_waitcnt lgkmcnt(4)
	v_add_f32_e32 v223, v223, v239
	s_waitcnt lgkmcnt(3)
	v_add_f32_e32 v224, v224, v240
	s_waitcnt lgkmcnt(2)
	v_add_f32_e32 v225, v225, v241
	s_waitcnt lgkmcnt(1)
	v_add_f32_e32 v226, v226, v242
	s_waitcnt lgkmcnt(0)
	v_add_f32_e32 v227, v227, v243
	ds_bpermute_b32 v244, v131, v228
	ds_bpermute_b32 v245, v131, v229
	ds_bpermute_b32 v246, v131, v230
	ds_bpermute_b32 v247, v131, v231
	ds_bpermute_b32 v248, v131, v232
	ds_bpermute_b32 v249, v131, v233
	ds_bpermute_b32 v250, v131, v234
	ds_bpermute_b32 v251, v131, v235
	s_waitcnt lgkmcnt(7)
	v_add_f32_e32 v228, v228, v244
	s_waitcnt lgkmcnt(6)
	v_add_f32_e32 v229, v229, v245
	s_waitcnt lgkmcnt(5)
	v_add_f32_e32 v230, v230, v246
	s_waitcnt lgkmcnt(4)
	v_add_f32_e32 v231, v231, v247
	s_waitcnt lgkmcnt(3)
	v_add_f32_e32 v232, v232, v248
	s_waitcnt lgkmcnt(2)
	v_add_f32_e32 v233, v233, v249
	s_waitcnt lgkmcnt(1)
	v_add_f32_e32 v234, v234, v250
	s_waitcnt lgkmcnt(0)
	v_add_f32_e32 v235, v235, v251
	s_and_saveexec_b64 s[4:5], s[0:1]
	ds_write_b32 v1, v220
	ds_write_b32 v1, v221 offset:16
	ds_write_b32 v165, v222
	ds_write_b32 v165, v223 offset:16
	ds_write_b32 v169, v224
	ds_write_b32 v169, v225 offset:16
	ds_write_b32 v173, v226
	ds_write_b32 v173, v227 offset:16
	ds_write_b32 v218, v228
	ds_write_b32 v218, v229 offset:16
	ds_write_b32 v183, v230
	ds_write_b32 v183, v231 offset:16
	ds_write_b32 v188, v232
	ds_write_b32 v188, v233 offset:16
	ds_write_b32 v190, v234
	ds_write_b32 v190, v235 offset:16
	s_or_b64 exec, exec, s[4:5]
	s_waitcnt lgkmcnt(0)
	s_barrier
	s_waitcnt lgkmcnt(0)
	ds_read_b128 v[130:133], v159
	ds_read_b128 v[134:137], v159 offset:16
	s_cmp_gt_i32 s22, 15
	s_cselect_b64 s[4:5], -1, 0
	v_cndmask_b32_e64 v179, 1.0, v199, s[4:5]
	s_waitcnt lgkmcnt(0)
	v_mov_b32_e32 v150, v131
	v_mov_b32_e32 v151, v132
	v_mov_b32_e32 v131, v133
	v_pk_add_f32 v[130:131], v[150:151], v[130:131]
	v_readlane_b32 s60, v254, 12
	v_add_f32_e32 v130, v130, v131
	v_fmamk_f32 v130, v130, 0x3c000000, v195
	v_mul_f32_e32 v131, 0x4f800000, v130
	v_cmp_gt_f32_e32 vcc, s76, v130
	v_readlane_b32 s61, v254, 13
	v_readlane_b32 s64, v254, 16
	v_cndmask_b32_e32 v130, v130, v131, vcc
	v_sqrt_f32_e32 v131, v130
	v_readlane_b32 s65, v254, 17
	v_readlane_b32 s66, v254, 18
	v_readlane_b32 s67, v254, 19
	v_add_u32_e32 v132, -1, v131
	v_fma_f32 v133, -v132, v131, v130
	v_cmp_ge_f32_e64 s[4:5], 0, v133
	v_add_u32_e32 v133, 1, v131
	v_readlane_b32 s70, v254, 22
	v_cndmask_b32_e64 v132, v131, v132, s[4:5]
	v_fma_f32 v131, -v133, v131, v130
	v_cmp_lt_f32_e64 s[4:5], 0, v131
	v_readlane_b32 s71, v254, 23
	s_cmp_lt_i32 s22, 8
	v_cndmask_b32_e64 v131, v132, v133, s[4:5]
	v_mul_f32_e32 v132, 0x37800000, v131
	v_cndmask_b32_e32 v131, v131, v132, vcc
	v_cmp_class_f32_e32 vcc, v130, v196
	s_mov_b64 s[60:61], s[64:65]
	s_mov_b64 s[66:67], s[70:71]
	v_cndmask_b32_e32 v132, v131, v130, vcc
	v_div_scale_f32 v133, s[4:5], v132, v132, v179
	v_rcp_f32_e32 v150, v133
	v_mov_b32_e32 v131, v136
	v_div_scale_f32 v151, vcc, v179, v132, v179
	v_fma_f32 v130, -v133, v150, 1.0
	v_fmac_f32_e32 v150, v130, v150
	v_mov_b32_e32 v130, v135
	v_mov_b32_e32 v135, v137
	v_pk_add_f32 v[130:131], v[130:131], v[134:135]
	v_mul_f32_e32 v152, v151, v150
	v_add_f32_e32 v130, v130, v131
	v_fmamk_f32 v130, v130, 0x3c000000, v195
	v_mul_f32_e32 v131, 0x4f800000, v130
	v_cmp_gt_f32_e64 s[4:5], s76, v130
	v_fma_f32 v134, -v133, v152, v151
	v_fmac_f32_e32 v152, v134, v150
	v_cndmask_b32_e64 v130, v130, v131, s[4:5]
	v_sqrt_f32_e32 v131, v130
	v_fma_f32 v133, -v133, v152, v151
	ds_read_b128 v[200:203], v189
	v_readlane_b32 s62, v254, 14
	v_add_u32_e32 v134, -1, v131
	v_fma_f32 v135, -v134, v131, v130
	v_cmp_ge_f32_e64 s[8:9], 0, v135
	v_add_u32_e32 v135, 1, v131
	v_readlane_b32 s63, v254, 15
	v_cndmask_b32_e64 v134, v131, v134, s[8:9]
	v_fma_f32 v131, -v135, v131, v130
	v_cmp_lt_f32_e64 s[8:9], 0, v131
	v_readlane_b32 s68, v254, 20
	v_readlane_b32 s69, v254, 21
	v_cndmask_b32_e64 v131, v134, v135, s[8:9]
	v_mul_f32_e32 v134, 0x37800000, v131
	v_cndmask_b32_e64 v131, v131, v134, s[4:5]
	v_cmp_class_f32_e64 s[4:5], v130, v196
	ds_read_b128 v[134:137], v163 offset:16
	v_readlane_b32 s72, v254, 24
	v_cndmask_b32_e64 v153, v131, v130, s[4:5]
	v_div_scale_f32 v154, s[4:5], v153, v153, v179
	v_rcp_f32_e32 v156, v154
	v_div_fmas_f32 v130, v133, v150, v152
	v_div_fixup_f32 v178, v130, v132, v179
	v_div_scale_f32 v152, vcc, v179, v153, v179
	v_fma_f32 v130, -v154, v156, 1.0
	v_fmac_f32_e32 v156, v130, v156
	ds_read_b128 v[130:133], v163
	v_mul_f32_e32 v158, v152, v156
	v_readlane_b32 s73, v254, 25
	v_readlane_b32 s74, v254, 26
	v_readlane_b32 s75, v254, 27
	s_waitcnt lgkmcnt(0)
	v_mov_b32_e32 v150, v131
	v_mov_b32_e32 v151, v132
	v_mov_b32_e32 v131, v133
	v_pk_add_f32 v[130:131], v[150:151], v[130:131]
	v_fma_f32 v132, -v154, v158, v152
	v_add_f32_e32 v130, v130, v131
	v_fmamk_f32 v130, v130, 0x3c000000, v195
	v_mul_f32_e32 v131, 0x4f800000, v130
	v_cmp_gt_f32_e64 s[4:5], s76, v130
	v_fmac_f32_e32 v158, v132, v156
	v_fma_f32 v132, -v154, v158, v152
	v_cndmask_b32_e64 v130, v130, v131, s[4:5]
	v_sqrt_f32_e32 v131, v130
	s_nop 0
	v_add_u32_e32 v133, -1, v131
	v_fma_f32 v150, -v133, v131, v130
	v_cmp_ge_f32_e64 s[8:9], 0, v150
	v_add_u32_e32 v150, 1, v131
	s_nop 0
	v_cndmask_b32_e64 v133, v131, v133, s[8:9]
	v_fma_f32 v131, -v150, v131, v130
	v_cmp_lt_f32_e64 s[8:9], 0, v131
	s_nop 1
	v_cndmask_b32_e64 v131, v133, v150, s[8:9]
	v_mul_f32_e32 v133, 0x37800000, v131
	v_cndmask_b32_e64 v131, v131, v133, s[4:5]
	v_cmp_class_f32_e64 s[4:5], v130, v196
	s_nop 1
	v_cndmask_b32_e64 v133, v131, v130, s[4:5]
	v_div_scale_f32 v150, s[4:5], v133, v133, v179
	v_rcp_f32_e32 v151, v150
	v_div_fmas_f32 v130, v132, v156, v158
	v_div_fixup_f32 v176, v130, v153, v179
	v_mov_b32_e32 v131, v136
	v_fma_f32 v130, -v150, v151, 1.0
	v_fmac_f32_e32 v151, v130, v151
	v_mov_b32_e32 v130, v135
	v_mov_b32_e32 v135, v137
	v_pk_add_f32 v[130:131], v[130:131], v[134:135]
	v_div_scale_f32 v132, vcc, v179, v133, v179
	v_add_f32_e32 v130, v130, v131
	v_fmamk_f32 v130, v130, 0x3c000000, v195
	v_mul_f32_e32 v131, 0x4f800000, v130
	v_cmp_gt_f32_e64 s[4:5], s76, v130
	v_mul_f32_e32 v152, v132, v151
	v_fma_f32 v134, -v150, v152, v132
	v_cndmask_b32_e64 v130, v130, v131, s[4:5]
	v_sqrt_f32_e32 v131, v130
	v_fmac_f32_e32 v152, v134, v151
	v_fma_f32 v132, -v150, v152, v132
	v_add_u32_e32 v134, -1, v131
	v_fma_f32 v135, -v134, v131, v130
	v_cmp_ge_f32_e64 s[8:9], 0, v135
	v_add_u32_e32 v135, 1, v131
	s_nop 0
	v_cndmask_b32_e64 v134, v131, v134, s[8:9]
	v_fma_f32 v131, -v135, v131, v130
	v_cmp_lt_f32_e64 s[8:9], 0, v131
	s_nop 1
	v_cndmask_b32_e64 v131, v134, v135, s[8:9]
	v_mul_f32_e32 v134, 0x37800000, v131
	v_cndmask_b32_e64 v131, v131, v134, s[4:5]
	v_cmp_class_f32_e64 s[4:5], v130, v196
	ds_read_b128 v[134:137], v167 offset:16
	s_nop 0
	v_cndmask_b32_e64 v153, v131, v130, s[4:5]
	v_div_scale_f32 v154, s[4:5], v153, v153, v179
	v_rcp_f32_e32 v156, v154
	v_div_fmas_f32 v130, v132, v151, v152
	v_div_fixup_f32 v174, v130, v133, v179
	v_div_scale_f32 v152, vcc, v179, v153, v179
	v_fma_f32 v130, -v154, v156, 1.0
	v_fmac_f32_e32 v156, v130, v156
	ds_read_b128 v[130:133], v167
	v_mul_f32_e32 v158, v152, v156
	s_waitcnt lgkmcnt(0)
	v_mov_b32_e32 v150, v131
	v_mov_b32_e32 v151, v132
	v_mov_b32_e32 v131, v133
	v_pk_add_f32 v[130:131], v[150:151], v[130:131]
	v_fma_f32 v132, -v154, v158, v152
	v_add_f32_e32 v130, v130, v131
	v_fmamk_f32 v130, v130, 0x3c000000, v195
	v_mul_f32_e32 v131, 0x4f800000, v130
	v_cmp_gt_f32_e64 s[4:5], s76, v130
	v_fmac_f32_e32 v158, v132, v156
	v_fma_f32 v132, -v154, v158, v152
	v_cndmask_b32_e64 v130, v130, v131, s[4:5]
	v_sqrt_f32_e32 v131, v130
	s_nop 0
	v_add_u32_e32 v133, -1, v131
	v_fma_f32 v150, -v133, v131, v130
	v_cmp_ge_f32_e64 s[8:9], 0, v150
	v_add_u32_e32 v150, 1, v131
	s_nop 0
	v_cndmask_b32_e64 v133, v131, v133, s[8:9]
	v_fma_f32 v131, -v150, v131, v130
	v_cmp_lt_f32_e64 s[8:9], 0, v131
	s_nop 1
	v_cndmask_b32_e64 v131, v133, v150, s[8:9]
	v_mul_f32_e32 v133, 0x37800000, v131
	v_cndmask_b32_e64 v131, v131, v133, s[4:5]
	v_cmp_class_f32_e64 s[4:5], v130, v196
	s_nop 1
	v_cndmask_b32_e64 v133, v131, v130, s[4:5]
	v_div_scale_f32 v150, s[4:5], v133, v133, v179
	v_rcp_f32_e32 v151, v150
	v_div_fmas_f32 v130, v132, v156, v158
	v_div_fixup_f32 v172, v130, v153, v179
	v_mov_b32_e32 v131, v136
	v_fma_f32 v130, -v150, v151, 1.0
	v_fmac_f32_e32 v151, v130, v151
	v_mov_b32_e32 v130, v135
	v_mov_b32_e32 v135, v137
	v_pk_add_f32 v[130:131], v[130:131], v[134:135]
	v_div_scale_f32 v132, vcc, v179, v133, v179
	v_add_f32_e32 v130, v130, v131
	v_fmamk_f32 v130, v130, 0x3c000000, v195
	v_mul_f32_e32 v131, 0x4f800000, v130
	v_cmp_gt_f32_e64 s[4:5], s76, v130
	v_mul_f32_e32 v152, v132, v151
	v_fma_f32 v134, -v150, v152, v132
	v_cndmask_b32_e64 v130, v130, v131, s[4:5]
	v_sqrt_f32_e32 v131, v130
	v_fmac_f32_e32 v152, v134, v151
	v_fma_f32 v132, -v150, v152, v132
	v_add_u32_e32 v134, -1, v131
	v_fma_f32 v135, -v134, v131, v130
	v_cmp_ge_f32_e64 s[8:9], 0, v135
	v_add_u32_e32 v135, 1, v131
	s_nop 0
	v_cndmask_b32_e64 v134, v131, v134, s[8:9]
	v_fma_f32 v131, -v135, v131, v130
	v_cmp_lt_f32_e64 s[8:9], 0, v131
	s_nop 1
	v_cndmask_b32_e64 v131, v134, v135, s[8:9]
	v_mul_f32_e32 v134, 0x37800000, v131
	v_cndmask_b32_e64 v131, v131, v134, s[4:5]
	v_cmp_class_f32_e64 s[4:5], v130, v196
	ds_read_b128 v[134:137], v171 offset:16
	s_nop 0
	v_cndmask_b32_e64 v153, v131, v130, s[4:5]
	v_div_scale_f32 v154, s[4:5], v153, v153, v179
	v_rcp_f32_e32 v156, v154
	v_div_fmas_f32 v130, v132, v151, v152
	v_div_fixup_f32 v170, v130, v133, v179
	v_div_scale_f32 v152, vcc, v179, v153, v179
	v_fma_f32 v130, -v154, v156, 1.0
	v_fmac_f32_e32 v156, v130, v156
	ds_read_b128 v[130:133], v171
	v_mul_f32_e32 v158, v152, v156
	s_waitcnt lgkmcnt(0)
	v_mov_b32_e32 v150, v131
	v_mov_b32_e32 v151, v132
	v_mov_b32_e32 v131, v133
	v_pk_add_f32 v[130:131], v[150:151], v[130:131]
	v_fma_f32 v132, -v154, v158, v152
	v_add_f32_e32 v130, v130, v131
	v_fmamk_f32 v130, v130, 0x3c000000, v195
	v_mul_f32_e32 v131, 0x4f800000, v130
	v_cmp_gt_f32_e64 s[4:5], s76, v130
	v_fmac_f32_e32 v158, v132, v156
	v_fma_f32 v132, -v154, v158, v152
	v_cndmask_b32_e64 v130, v130, v131, s[4:5]
	v_sqrt_f32_e32 v131, v130
	s_nop 0
	v_add_u32_e32 v133, -1, v131
	v_fma_f32 v150, -v133, v131, v130
	v_cmp_ge_f32_e64 s[8:9], 0, v150
	v_add_u32_e32 v150, 1, v131
	s_nop 0
	v_cndmask_b32_e64 v133, v131, v133, s[8:9]
	v_fma_f32 v131, -v150, v131, v130
	v_cmp_lt_f32_e64 s[8:9], 0, v131
	s_nop 1
	v_cndmask_b32_e64 v131, v133, v150, s[8:9]
	v_mul_f32_e32 v133, 0x37800000, v131
	v_cndmask_b32_e64 v131, v131, v133, s[4:5]
	v_cmp_class_f32_e64 s[4:5], v130, v196
	s_nop 1
	v_cndmask_b32_e64 v133, v131, v130, s[4:5]
	v_div_scale_f32 v150, s[4:5], v133, v133, v179
	v_rcp_f32_e32 v151, v150
	v_div_fmas_f32 v130, v132, v156, v158
	v_div_fixup_f32 v168, v130, v153, v179
	v_mov_b32_e32 v131, v136
	v_fma_f32 v130, -v150, v151, 1.0
	v_fmac_f32_e32 v151, v130, v151
	v_mov_b32_e32 v130, v135
	v_mov_b32_e32 v135, v137
	v_pk_add_f32 v[130:131], v[130:131], v[134:135]
	v_div_scale_f32 v132, vcc, v179, v133, v179
	v_add_f32_e32 v130, v130, v131
	v_fmamk_f32 v130, v130, 0x3c000000, v195
	v_mul_f32_e32 v131, 0x4f800000, v130
	v_cmp_gt_f32_e64 s[4:5], s76, v130
	v_mul_f32_e32 v152, v132, v151
	v_fma_f32 v134, -v150, v152, v132
	v_cndmask_b32_e64 v130, v130, v131, s[4:5]
	v_sqrt_f32_e32 v131, v130
	v_fmac_f32_e32 v152, v134, v151
	v_fma_f32 v132, -v150, v152, v132
	v_add_u32_e32 v134, -1, v131
	v_fma_f32 v135, -v134, v131, v130
	v_cmp_ge_f32_e64 s[8:9], 0, v135
	v_add_u32_e32 v135, 1, v131
	s_nop 0
	v_cndmask_b32_e64 v134, v131, v134, s[8:9]
	v_fma_f32 v131, -v135, v131, v130
	v_cmp_lt_f32_e64 s[8:9], 0, v131
	s_nop 1
	v_cndmask_b32_e64 v131, v134, v135, s[8:9]
	v_mul_f32_e32 v134, 0x37800000, v131
	v_cndmask_b32_e64 v131, v131, v134, s[4:5]
	v_cmp_class_f32_e64 s[4:5], v130, v196
	ds_read_b128 v[134:137], v175 offset:16
	s_nop 0
	v_cndmask_b32_e64 v153, v131, v130, s[4:5]
	v_div_scale_f32 v154, s[4:5], v153, v153, v179
	v_rcp_f32_e32 v156, v154
	v_div_fmas_f32 v130, v132, v151, v152
	v_div_fixup_f32 v166, v130, v133, v179
	v_div_scale_f32 v152, vcc, v179, v153, v179
	v_fma_f32 v130, -v154, v156, 1.0
	v_fmac_f32_e32 v156, v130, v156
	ds_read_b128 v[130:133], v175
	v_mul_f32_e32 v158, v152, v156
	s_waitcnt lgkmcnt(0)
	v_mov_b32_e32 v150, v131
	v_mov_b32_e32 v151, v132
	v_mov_b32_e32 v131, v133
	v_pk_add_f32 v[130:131], v[150:151], v[130:131]
	v_fma_f32 v132, -v154, v158, v152
	v_add_f32_e32 v130, v130, v131
	v_fmamk_f32 v130, v130, 0x3c000000, v195
	v_mul_f32_e32 v131, 0x4f800000, v130
	v_cmp_gt_f32_e64 s[4:5], s76, v130
	v_fmac_f32_e32 v158, v132, v156
	v_fma_f32 v132, -v154, v158, v152
	v_cndmask_b32_e64 v130, v130, v131, s[4:5]
	v_sqrt_f32_e32 v131, v130
	s_nop 0
	v_add_u32_e32 v133, -1, v131
	v_fma_f32 v150, -v133, v131, v130
	v_cmp_ge_f32_e64 s[8:9], 0, v150
	v_add_u32_e32 v150, 1, v131
	s_nop 0
	v_cndmask_b32_e64 v133, v131, v133, s[8:9]
	v_fma_f32 v131, -v150, v131, v130
	v_cmp_lt_f32_e64 s[8:9], 0, v131
	s_nop 1
	v_cndmask_b32_e64 v131, v133, v150, s[8:9]
	v_mul_f32_e32 v133, 0x37800000, v131
	v_cndmask_b32_e64 v131, v131, v133, s[4:5]
	v_cmp_class_f32_e64 s[4:5], v130, v196
	s_nop 1
	v_cndmask_b32_e64 v133, v131, v130, s[4:5]
	v_div_scale_f32 v150, s[4:5], v133, v133, v179
	v_rcp_f32_e32 v151, v150
	v_div_fmas_f32 v130, v132, v156, v158
	v_div_fixup_f32 v164, v130, v153, v179
	v_mov_b32_e32 v131, v136
	v_fma_f32 v130, -v150, v151, 1.0
	v_fmac_f32_e32 v151, v130, v151
	v_mov_b32_e32 v130, v135
	v_mov_b32_e32 v135, v137
	v_pk_add_f32 v[130:131], v[130:131], v[134:135]
	v_div_scale_f32 v132, vcc, v179, v133, v179
	v_add_f32_e32 v130, v130, v131
	v_fmamk_f32 v130, v130, 0x3c000000, v195
	v_mul_f32_e32 v131, 0x4f800000, v130
	v_cmp_gt_f32_e64 s[4:5], s76, v130
	v_mul_f32_e32 v152, v132, v151
	v_fma_f32 v134, -v150, v152, v132
	v_cndmask_b32_e64 v130, v130, v131, s[4:5]
	v_sqrt_f32_e32 v131, v130
	v_fmac_f32_e32 v152, v134, v151
	v_fma_f32 v132, -v150, v152, v132
	v_add_u32_e32 v134, -1, v131
	v_fma_f32 v135, -v134, v131, v130
	v_cmp_ge_f32_e64 s[8:9], 0, v135
	v_add_u32_e32 v135, 1, v131
	s_nop 0
	v_cndmask_b32_e64 v134, v131, v134, s[8:9]
	v_fma_f32 v131, -v135, v131, v130
	v_cmp_lt_f32_e64 s[8:9], 0, v131
	s_nop 1
	v_cndmask_b32_e64 v131, v134, v135, s[8:9]
	v_mul_f32_e32 v134, 0x37800000, v131
	v_cndmask_b32_e64 v131, v131, v134, s[4:5]
	v_cmp_class_f32_e64 s[4:5], v130, v196
	ds_read_b128 v[134:137], v181 offset:16
	s_nop 0
	v_cndmask_b32_e64 v153, v131, v130, s[4:5]
	v_div_scale_f32 v154, s[4:5], v153, v153, v179
	v_rcp_f32_e32 v156, v154
	v_div_fmas_f32 v130, v132, v151, v152
	v_div_fixup_f32 v162, v130, v133, v179
	v_div_scale_f32 v152, vcc, v179, v153, v179
	v_fma_f32 v130, -v154, v156, 1.0
	v_fmac_f32_e32 v156, v130, v156
	ds_read_b128 v[130:133], v181
	v_mul_f32_e32 v158, v152, v156
	s_waitcnt lgkmcnt(0)
	v_mov_b32_e32 v150, v131
	v_mov_b32_e32 v151, v132
	v_mov_b32_e32 v131, v133
	v_pk_add_f32 v[130:131], v[150:151], v[130:131]
	v_fma_f32 v132, -v154, v158, v152
	v_add_f32_e32 v130, v130, v131
	v_fmamk_f32 v130, v130, 0x3c000000, v195
	v_mul_f32_e32 v131, 0x4f800000, v130
	v_cmp_gt_f32_e64 s[4:5], s76, v130
	v_fmac_f32_e32 v158, v132, v156
	v_fma_f32 v132, -v154, v158, v152
	v_cndmask_b32_e64 v130, v130, v131, s[4:5]
	v_sqrt_f32_e32 v131, v130
	s_nop 0
	v_add_u32_e32 v133, -1, v131
	v_fma_f32 v150, -v133, v131, v130
	v_cmp_ge_f32_e64 s[8:9], 0, v150
	v_add_u32_e32 v150, 1, v131
	s_nop 0
	v_cndmask_b32_e64 v133, v131, v133, s[8:9]
	v_fma_f32 v131, -v150, v131, v130
	v_cmp_lt_f32_e64 s[8:9], 0, v131
	s_nop 1
	v_cndmask_b32_e64 v131, v133, v150, s[8:9]
	v_mul_f32_e32 v133, 0x37800000, v131
	v_cndmask_b32_e64 v131, v131, v133, s[4:5]
	v_cmp_class_f32_e64 s[4:5], v130, v196
	s_nop 1
	v_cndmask_b32_e64 v133, v131, v130, s[4:5]
	v_div_scale_f32 v150, s[4:5], v133, v133, v179
	v_rcp_f32_e32 v151, v150
	v_div_fmas_f32 v130, v132, v156, v158
	v_div_fixup_f32 v160, v130, v153, v179
	v_mov_b32_e32 v131, v136
	v_fma_f32 v130, -v150, v151, 1.0
	v_fmac_f32_e32 v151, v130, v151
	v_mov_b32_e32 v130, v135
	v_mov_b32_e32 v135, v137
	v_pk_add_f32 v[130:131], v[130:131], v[134:135]
	v_div_scale_f32 v132, vcc, v179, v133, v179
	v_add_f32_e32 v130, v130, v131
	v_fmamk_f32 v130, v130, 0x3c000000, v195
	v_mul_f32_e32 v131, 0x4f800000, v130
	v_cmp_gt_f32_e64 s[4:5], s76, v130
	v_mul_f32_e32 v152, v132, v151
	v_fma_f32 v134, -v150, v152, v132
	v_cndmask_b32_e64 v130, v130, v131, s[4:5]
	v_sqrt_f32_e32 v131, v130
	v_fmac_f32_e32 v152, v134, v151
	v_fma_f32 v132, -v150, v152, v132
	v_add_u32_e32 v134, -1, v131
	v_fma_f32 v135, -v134, v131, v130
	v_cmp_ge_f32_e64 s[8:9], 0, v135
	v_add_u32_e32 v135, 1, v131
	s_nop 0
	v_cndmask_b32_e64 v134, v131, v134, s[8:9]
	v_fma_f32 v131, -v135, v131, v130
	v_cmp_lt_f32_e64 s[8:9], 0, v131
	s_nop 1
	v_cndmask_b32_e64 v131, v134, v135, s[8:9]
	v_mul_f32_e32 v134, 0x37800000, v131
	v_cndmask_b32_e64 v131, v131, v134, s[4:5]
	v_cmp_class_f32_e64 s[4:5], v130, v196
	ds_read_b128 v[134:137], v185 offset:16
	s_nop 0
	v_cndmask_b32_e64 v153, v131, v130, s[4:5]
	v_div_scale_f32 v154, s[4:5], v153, v153, v179
	v_rcp_f32_e32 v156, v154
	v_div_fmas_f32 v130, v132, v151, v152
	v_div_fixup_f32 v158, v130, v133, v179
	v_div_scale_f32 v152, vcc, v179, v153, v179
	v_fma_f32 v130, -v154, v156, 1.0
	v_fmac_f32_e32 v156, v130, v156
	ds_read_b128 v[130:133], v185
	v_mul_f32_e32 v161, v152, v156
	s_waitcnt lgkmcnt(0)
	v_mov_b32_e32 v150, v131
	v_mov_b32_e32 v151, v132
	v_mov_b32_e32 v131, v133
	v_pk_add_f32 v[130:131], v[150:151], v[130:131]
	v_fma_f32 v132, -v154, v161, v152
	v_add_f32_e32 v130, v130, v131
	v_fmamk_f32 v130, v130, 0x3c000000, v195
	v_mul_f32_e32 v131, 0x4f800000, v130
	v_cmp_gt_f32_e64 s[4:5], s76, v130
	v_fmac_f32_e32 v161, v132, v156
	v_fma_f32 v132, -v154, v161, v152
	v_cndmask_b32_e64 v130, v130, v131, s[4:5]
	v_sqrt_f32_e32 v131, v130
	s_nop 0
	v_add_u32_e32 v133, -1, v131
	v_fma_f32 v150, -v133, v131, v130
	v_cmp_ge_f32_e64 s[8:9], 0, v150
	v_add_u32_e32 v150, 1, v131
	s_nop 0
	v_cndmask_b32_e64 v133, v131, v133, s[8:9]
	v_fma_f32 v131, -v150, v131, v130
	v_cmp_lt_f32_e64 s[8:9], 0, v131
	s_nop 1
	v_cndmask_b32_e64 v131, v133, v150, s[8:9]
	v_mul_f32_e32 v133, 0x37800000, v131
	v_cndmask_b32_e64 v131, v131, v133, s[4:5]
	v_cmp_class_f32_e64 s[4:5], v130, v196
	s_nop 1
	v_cndmask_b32_e64 v133, v131, v130, s[4:5]
	v_div_scale_f32 v150, s[4:5], v133, v133, v179
	v_rcp_f32_e32 v151, v150
	v_div_fmas_f32 v130, v132, v156, v161
	v_div_fixup_f32 v156, v130, v153, v179
	v_mov_b32_e32 v131, v136
	v_fma_f32 v130, -v150, v151, 1.0
	v_fmac_f32_e32 v151, v130, v151
	v_mov_b32_e32 v130, v135
	v_mov_b32_e32 v135, v137
	v_pk_add_f32 v[130:131], v[130:131], v[134:135]
	v_div_scale_f32 v132, vcc, v179, v133, v179
	v_add_f32_e32 v130, v130, v131
	v_fmamk_f32 v130, v130, 0x3c000000, v195
	v_mul_f32_e32 v131, 0x4f800000, v130
	v_cmp_gt_f32_e64 s[4:5], s76, v130
	v_mul_f32_e32 v152, v132, v151
	v_fma_f32 v134, -v150, v152, v132
	v_cndmask_b32_e64 v130, v130, v131, s[4:5]
	v_sqrt_f32_e32 v131, v130
	v_fmac_f32_e32 v152, v134, v151
	v_fma_f32 v132, -v150, v152, v132
	v_mov_b32_e32 v150, v201
	v_add_u32_e32 v134, -1, v131
	v_fma_f32 v135, -v134, v131, v130
	v_cmp_ge_f32_e64 s[8:9], 0, v135
	v_add_u32_e32 v135, 1, v131
	v_mov_b32_e32 v201, v203
	v_cndmask_b32_e64 v134, v131, v134, s[8:9]
	v_fma_f32 v131, -v135, v131, v130
	v_cmp_lt_f32_e64 s[8:9], 0, v131
	s_nop 1
	v_cndmask_b32_e64 v131, v134, v135, s[8:9]
	v_mul_f32_e32 v134, 0x37800000, v131
	v_cndmask_b32_e64 v131, v131, v134, s[4:5]
	v_cmp_class_f32_e64 s[4:5], v130, v196
	s_nop 1
	v_cndmask_b32_e64 v153, v131, v130, s[4:5]
	v_div_scale_f32 v161, s[4:5], v153, v153, v179
	v_rcp_f32_e32 v177, v161
	s_cselect_b32 s4, s60, s66
	v_div_fmas_f32 v130, v132, v151, v152
	s_cselect_b32 s5, s61, s67
	s_add_u32 s4, s4, s77
	v_div_fixup_f32 v154, v130, v133, v179
	v_fma_f32 v130, -v161, v177, 1.0
	s_addc_u32 s5, s5, 0
	v_fmac_f32_e32 v177, v130, v177
	global_load_dwordx4 v[134:137], v197, s[4:5]
	global_load_dwordx4 v[130:133], v197, s[4:5] offset:16
	v_mov_b32_e32 v151, v202
	v_pk_add_f32 v[150:151], v[150:151], v[200:201]
	v_div_scale_f32 v152, vcc, v179, v153, v179
	v_add_f32_e32 v150, v150, v151
	v_fmamk_f32 v150, v150, 0x3c000000, v195
	v_mul_f32_e32 v151, 0x4f800000, v150
	v_cmp_gt_f32_e64 s[4:5], s76, v150
	v_mul_f32_e32 v180, v152, v177
	v_fma_f32 v182, -v161, v180, v152
	v_cndmask_b32_e64 v150, v150, v151, s[4:5]
	v_sqrt_f32_e32 v151, v150
	v_fmac_f32_e32 v180, v182, v177
	v_fma_f32 v152, -v161, v180, v152
	ds_read_b128 v[204:207], v189 offset:16
	v_add_u32_e32 v161, -1, v151
	v_fma_f32 v182, -v161, v151, v150
	v_cmp_ge_f32_e64 s[8:9], 0, v182
	v_add_u32_e32 v182, 1, v151
	s_nop 0
	v_cndmask_b32_e64 v161, v151, v161, s[8:9]
	v_fma_f32 v151, -v182, v151, v150
	v_cmp_lt_f32_e64 s[8:9], 0, v151
	s_nop 1
	v_cndmask_b32_e64 v151, v161, v182, s[8:9]
	v_mul_f32_e32 v161, 0x37800000, v151
	v_cndmask_b32_e64 v151, v151, v161, s[4:5]
	v_cmp_class_f32_e64 s[4:5], v150, v196
	s_nop 1
	v_cndmask_b32_e64 v161, v151, v150, s[4:5]
	v_div_scale_f32 v182, s[4:5], v161, v161, v179
	v_rcp_f32_e32 v186, v182
	v_div_fmas_f32 v150, v152, v177, v180
	v_div_fixup_f32 v184, v150, v153, v179
	s_waitcnt lgkmcnt(0)
	v_mov_b32_e32 v151, v206
	v_fma_f32 v150, -v182, v186, 1.0
	v_fmac_f32_e32 v186, v150, v186
	v_mov_b32_e32 v150, v205
	v_mov_b32_e32 v205, v207
	v_pk_add_f32 v[150:151], v[150:151], v[204:205]
	v_div_scale_f32 v152, vcc, v179, v161, v179
	v_add_f32_e32 v150, v150, v151
	v_fmamk_f32 v150, v150, 0x3c000000, v195
	v_mul_f32_e32 v151, 0x4f800000, v150
	v_cmp_gt_f32_e64 s[4:5], s76, v150
	v_mul_f32_e32 v153, v152, v186
	v_fma_f32 v177, -v182, v153, v152
	v_cndmask_b32_e64 v150, v150, v151, s[4:5]
	v_sqrt_f32_e32 v151, v150
	v_fmac_f32_e32 v153, v177, v186
	v_fma_f32 v152, -v182, v153, v152
	v_div_fmas_f32 v152, v152, v186, v153
	v_add_u32_e32 v177, -1, v151
	v_fma_f32 v180, -v177, v151, v150
	v_cmp_ge_f32_e64 s[8:9], 0, v180
	v_add_u32_e32 v180, 1, v151
	v_div_fixup_f32 v182, v152, v161, v179
	v_cndmask_b32_e64 v177, v151, v177, s[8:9]
	v_fma_f32 v151, -v180, v151, v150
	v_cmp_lt_f32_e64 s[8:9], 0, v151
	s_nop 1
	v_cndmask_b32_e64 v151, v177, v180, s[8:9]
	v_mul_f32_e32 v177, 0x37800000, v151
	v_cndmask_b32_e64 v151, v151, v177, s[4:5]
	v_cmp_class_f32_e64 s[4:5], v150, v196
	s_nop 1
	v_cndmask_b32_e64 v150, v151, v150, s[4:5]
	v_div_scale_f32 v151, s[4:5], v150, v150, v179
	v_rcp_f32_e32 v177, v151
	s_nop 0
	v_fma_f32 v152, -v151, v177, 1.0
	v_fmac_f32_e32 v177, v152, v177
	v_div_scale_f32 v152, vcc, v179, v150, v179
	v_mul_f32_e32 v153, v152, v177
	v_fma_f32 v161, -v151, v153, v152
	v_fmac_f32_e32 v153, v161, v177
	v_fma_f32 v151, -v151, v153, v152
	v_div_fmas_f32 v151, v151, v177, v153
	v_div_fixup_f32 v180, v151, v150, v179
